# batch 3 plus N1: the two rows' residual (bf16) loads of layer 1 are issued together before the first wait (the compiler waited for row 0 before issuing row 1)
# baseline (speedup 1.0000x reference)
; DI float bflo(unsigned w) { return __uint_as_float(w << 16); }
; DI float bfhi(unsigned w) { return __uint_as_float(w & 0xffff0000u); }
; DI void load_row_bf16(const bf16_t* p, int lane, f32x4 (&v)[4]) {
; #pragma unroll
;     for (int j = 0; j < 4; ++j) { const u32x2 w = *(const u32x2*)(p + 4 * lane + 256 * j); v[j][0] = bflo(w.x); v[j][1] = bfhi(w.x); v[j][2] = bflo(w.y); v[j][3] = bfhi(w.y); }
; }
; DI void phase_n1(Frame& F, int l) {
;     ...
;     for (int blk = F.bid; blk < T / 16; blk += F.G) {
;         if (F.tid < 32) hist[F.tid] = 0;
;         f32x4 hv[2][4], yv2[2][4], xv2[2][4];
; #pragma unroll
;         for (int rr = 0; rr < 2; ++rr) { const int r = blk * 16 + F.wave * 2 + rr;
;             load_row_bf16(ymix + (size_t)r * D, F.lane, yv2[rr]); if (l == 0) load_row_f32(xin + (size_t)r * D, F.lane, xv2[rr]); else load_row_bf16(xb + (size_t)r * D, F.lane, xv2[rr]); }
.LBB0_1030:
	s_and_saveexec_b64 s[2:3], s[4:5]
	ds_write_b32 v147, v1
	s_or_b64 exec, exec, s[2:3]
	s_ashr_i32 s23, s22, 31
	s_lshl_b64 s[28:29], s[22:23], 11
	v_lshl_add_u64 v[2:3], v[98:99], 0, s[28:29]
	global_load_dwordx2 v[24:25], v[2:3], off nt
	global_load_dwordx2 v[22:23], v[2:3], off offset:512 nt
	global_load_dwordx2 v[20:21], v[2:3], off offset:1024 nt
	global_load_dwordx2 v[18:19], v[2:3], off offset:1536 nt
	v_readlane_b32 s0, v253, 23
	v_readlane_b32 s1, v253, 24
	s_lshl_b64 s[26:27], s[22:23], 10
	s_mov_b64 s[2:3], -1
	s_and_b64 vcc, exec, s[0:1]
	s_cbranch_vccz .LBB0_1034
	v_lshl_add_u64 v[2:3], s[26:27], 1, v[100:101]
	global_load_dwordx2 v[184:185], v[2:3], off nt
	global_load_dwordx2 v[186:187], v[2:3], off offset:512 nt
	global_load_dwordx2 v[188:189], v[2:3], off offset:1024 nt
	s_nop 0
	global_load_dwordx2 v[190:191], v[2:3], off offset:1536 nt
	s_mov_b64 s[2:3], 0

; DI float bflo(unsigned w) { return __uint_as_float(w << 16); }
; DI float bfhi(unsigned w) { return __uint_as_float(w & 0xffff0000u); }
; DI void load_row_bf16(const bf16_t* p, int lane, f32x4 (&v)[4]) {
; #pragma unroll
;     for (int j = 0; j < 4; ++j) { const u32x2 w = *(const u32x2*)(p + 4 * lane + 256 * j); v[j][0] = bflo(w.x); v[j][1] = bfhi(w.x); v[j][2] = bflo(w.y); v[j][3] = bfhi(w.y); }
; }
; DI void phase_n1(Frame& F, int l) {
;     ...
;         for (int rr = 0; rr < 2; ++rr) { const int r = blk * 16 + F.wave * 2 + rr;
;             load_row_bf16(ymix + (size_t)r * D, F.lane, yv2[rr]); if (l == 0) load_row_f32(xin + (size_t)r * D, F.lane, xv2[rr]); else load_row_bf16(xb + (size_t)r * D, F.lane, xv2[rr]); }
.LBB0_1036:
	s_add_i32 s0, s22, 1
	s_ashr_i32 s1, s0, 31
	s_lshl_b64 s[14:15], s[0:1], 11
	v_lshl_add_u64 v[2:3], v[98:99], 0, s[14:15]
	global_load_dwordx2 v[32:33], v[2:3], off nt
	global_load_dwordx2 v[30:31], v[2:3], off offset:512 nt
	global_load_dwordx2 v[28:29], v[2:3], off offset:1024 nt
	global_load_dwordx2 v[26:27], v[2:3], off offset:1536 nt
	s_lshl_b64 s[2:3], s[0:1], 10
	v_readlane_b32 s0, v253, 23
	v_readlane_b32 s1, v253, 24
	s_andn2_b64 vcc, exec, s[0:1]
	s_mov_b64 s[16:17], -1
	s_cbranch_vccnz .LBB0_1038
	v_lshl_add_u64 v[2:3], s[2:3], 1, v[100:101]
	global_load_dwordx2 v[192:193], v[2:3], off nt
	global_load_dwordx2 v[194:195], v[2:3], off offset:512 nt
	global_load_dwordx2 v[196:197], v[2:3], off offset:1024 nt
	global_load_dwordx2 v[198:199], v[2:3], off offset:1536 nt
	s_mov_b64 s[16:17], 0

; DI const float* inp(kptr_t k, int i) { return (const float*)k[i]; }
; DI void phase_n1(Frame& F, int l) {
;     ...
;         for (int rr = 0; rr < 2; ++rr) { const int r = blk * 16 + F.wave * 2 + rr;
;             load_row_bf16(ymix + (size_t)r * D, F.lane, yv2[rr]); if (l == 0) load_row_f32(xin + (size_t)r * D, F.lane, xv2[rr]); else load_row_bf16(xb + (size_t)r * D, F.lane, xv2[rr]); }
;         const float* mb = mod + (size_t)((blk * 16) / SEQ) * NMOD * D;
;         f32x4 gpm[4], gtm[4]; ModP mp;
; #pragma unroll
;         for (int j = 0; j < 4; ++j) { const int o = 4 * F.lane + 256 * j; gpm[j] = *(const f32x4*)(inp(KA, I_GPOSTMIX) + l * D + o); gtm[j] = *(const f32x4*)(mb + 2 * D + o); }
;         load_modp(mp, inp(KA, I_GPREFFN) + l * D, mb + 4 * D, mb + 3 * D, F.lane);
; #pragma unroll
;         for (int rr = 0; rr < 2; ++rr) { const int r = blk * 16 + F.wave * 2 + rr;
;             f32x4 (&yv)[4] = yv2[rr]; f32x4 (&xv)[4] = xv2[rr];
;             const float rstd_y = rsqrtf(sumsq(yv, F.lane) * (1.0f / D) + RMS_EPS);
.LBB0_1040:
	s_ashr_i32 s0, s30, 31
	s_lshr_b32 s0, s0, 25
	s_add_i32 s0, s30, s0
	s_ashr_i32 s0, s0, 7
	s_mul_i32 s0, s0, 6
	s_ashr_i32 s1, s0, 31
	s_lshl_b64 s[0:1], s[0:1], 12
	s_add_u32 s0, s31, s0
	s_addc_u32 s1, s33, s1
	v_lshl_add_u64 v[34:35], s[0:1], 0, v[110:111]
	s_movk_i32 s0, 0x4000
	v_add_co_u32_e32 v36, vcc, s0, v34
	s_mov_b64 s[0:1], 0x4000
	s_nop 0
	v_addc_co_u32_e32 v37, vcc, 0, v35, vcc
	global_load_dwordx4 v[112:115], v[36:37], off
	v_lshl_add_u64 v[36:37], v[34:35], 0, s[0:1]
	global_load_dwordx4 v[140:143], v[36:37], off offset:1024
	global_load_dwordx4 v[156:159], v[36:37], off offset:2048
	s_load_dwordx4 s[16:19], s[20:21], 0x30
	s_waitcnt vmcnt(0)
	v_readlane_b32 s100, v253, 23
	v_readlane_b32 s101, v253, 24
	s_nop 3
	s_cmp_eq_u64 s[100:101], 0
	s_cbranch_scc1 .Ln1_noup
	v_lshlrev_b32_e32 v62, 16, v184
	v_and_b32_e32 v63, 0xffff0000, v184
	v_lshlrev_b32_e32 v64, 16, v185
	v_and_b32_e32 v65, 0xffff0000, v185
	v_lshlrev_b32_e32 v58, 16, v186
	v_and_b32_e32 v59, 0xffff0000, v186
	v_lshlrev_b32_e32 v60, 16, v187
	v_and_b32_e32 v61, 0xffff0000, v187
	v_lshlrev_b32_e32 v50, 16, v188
	v_and_b32_e32 v51, 0xffff0000, v188
	v_lshlrev_b32_e32 v52, 16, v189
	v_and_b32_e32 v53, 0xffff0000, v189
	v_lshlrev_b32_e32 v38, 16, v190
	v_and_b32_e32 v39, 0xffff0000, v190
	v_lshlrev_b32_e32 v40, 16, v191
	v_and_b32_e32 v41, 0xffff0000, v191
	v_lshlrev_b32_e32 v14, 16, v192
	v_and_b32_e32 v15, 0xffff0000, v192
	v_lshlrev_b32_e32 v16, 16, v193
	v_and_b32_e32 v17, 0xffff0000, v193
	v_lshlrev_b32_e32 v10, 16, v194
	v_and_b32_e32 v11, 0xffff0000, v194
	v_lshlrev_b32_e32 v12, 16, v195
	v_and_b32_e32 v13, 0xffff0000, v195
	v_lshlrev_b32_e32 v6, 16, v196
	v_and_b32_e32 v7, 0xffff0000, v196
	v_lshlrev_b32_e32 v8, 16, v197
	v_and_b32_e32 v9, 0xffff0000, v197
	v_lshlrev_b32_e32 v2, 16, v198
	v_and_b32_e32 v3, 0xffff0000, v198
	v_lshlrev_b32_e32 v4, 16, v199
	v_and_b32_e32 v5, 0xffff0000, v199
.Ln1_noup:
	v_lshlrev_b32_e32 v169, 16, v23
	v_lshlrev_b32_e32 v168, 16, v22
	v_and_b32_e32 v171, 0xffff0000, v23
	v_and_b32_e32 v170, 0xffff0000, v22
	s_waitcnt lgkmcnt(0)
	s_add_u32 s0, s16, s24
	s_addc_u32 s1, s17, s25
	v_lshl_add_u64 v[22:23], s[0:1], 0, v[110:111]
	s_movk_i32 s0, 0x3000
	v_lshlrev_b32_e32 v172, 16, v20
	v_and_b32_e32 v173, 0xffff0000, v20
	v_add_co_u32_e32 v20, vcc, s0, v34
	v_lshlrev_b32_e32 v174, 16, v21
	v_and_b32_e32 v175, 0xffff0000, v21
	global_load_dwordx4 v[70:73], v[22:23], off
	global_load_dwordx4 v[94:97], v[22:23], off offset:1024
	v_addc_co_u32_e32 v21, vcc, 0, v35, vcc
	global_load_dwordx4 v[74:77], v[20:21], off offset:-4096
	v_and_b32_e32 v167, 0xffff0000, v25
	v_lshlrev_b32_e32 v166, 16, v25
	v_lshlrev_b32_e32 v177, 16, v18
	global_load_dwordx4 v[160:163], v[36:37], off offset:3072
	v_and_b32_e32 v179, 0xffff0000, v18
	v_mul_f32_e32 v18, v167, v167
	s_mov_b64 s[0:1], 0x2000
	v_lshlrev_b32_e32 v180, 16, v19
	v_and_b32_e32 v181, 0xffff0000, v19
	v_pk_fma_f32 v[144:145], v[166:167], v[166:167], v[18:19] op_sel_hi:[1,1,0]
	v_lshl_add_u64 v[18:19], v[34:35], 0, s[0:1]
	global_load_dwordx4 v[90:93], v[18:19], off offset:1024
	v_lshlrev_b32_e32 v164, 16, v24
	v_and_b32_e32 v165, 0xffff0000, v24
	v_pk_mul_f32 v[24:25], v[170:171], v[170:171]
	s_mov_b64 s[0:1], 0x3000
	v_lshlrev_b32_e32 v128, 16, v28
	v_and_b32_e32 v129, 0xffff0000, v28
	v_lshlrev_b32_e32 v130, 16, v29
	v_and_b32_e32 v131, 0xffff0000, v29
	v_lshlrev_b32_e32 v121, 16, v26
	v_and_b32_e32 v119, 0xffff0000, v26
	v_lshlrev_b32_e32 v122, 16, v27
	v_and_b32_e32 v123, 0xffff0000, v27
	v_pk_fma_f32 v[182:183], v[168:169], v[168:169], v[24:25]
	v_lshl_add_u64 v[24:25], v[34:35], 0, s[0:1]
	global_load_dwordx4 v[82:85], v[18:19], off offset:2048
	global_load_dwordx4 v[66:69], v[18:19], off offset:3072
	global_load_dwordx4 v[46:49], v[20:21], off
	global_load_dwordx4 v[86:89], v[22:23], off offset:2048
	global_load_dwordx4 v[34:37], v[24:25], off offset:1024
	global_load_dwordx4 v[26:29], v[24:25], off offset:2048
	s_nop 0
	global_load_dwordx4 v[18:21], v[24:25], off offset:3072
	global_load_dwordx4 v[78:81], v[22:23], off offset:3072
	s_add_u32 s0, s18, s24
	s_addc_u32 s1, s19, s25
	v_lshl_add_u64 v[22:23], s[0:1], 0, v[110:111]
	v_lshlrev_b32_e32 v136, 16, v32
	v_and_b32_e32 v137, 0xffff0000, v32
	v_lshlrev_b32_e32 v138, 16, v33
	v_and_b32_e32 v139, 0xffff0000, v33
	v_lshlrev_b32_e32 v133, 16, v31
	v_lshlrev_b32_e32 v132, 16, v30
	v_and_b32_e32 v135, 0xffff0000, v31
	v_and_b32_e32 v134, 0xffff0000, v30
	global_load_dwordx4 v[54:57], v[22:23], off
	global_load_dwordx4 v[42:45], v[22:23], off offset:1024
	global_load_dwordx4 v[30:33], v[22:23], off offset:2048
	s_nop 0
	global_load_dwordx4 v[22:25], v[22:23], off offset:3072
	v_mul_f32_e32 v118, v165, v165
	v_mul_f32_e32 v109, v179, v179
	v_mul_f32_e32 v120, v180, v180
	v_mul_f32_e32 v155, v181, v181
	v_mov_b32_e32 v178, v177
	v_pk_add_f32 v[124:125], v[114:115], 1.0 op_sel_hi:[1,0]
	v_pk_add_f32 v[116:117], v[140:141], 1.0 op_sel_hi:[1,0]
	v_pk_fma_f32 v[140:141], v[164:165], v[164:165], v[118:119] op_sel_hi:[1,1,0]
	v_pk_add_f32 v[114:115], v[142:143], 1.0 op_sel_hi:[1,0]
	v_mov_b32_e32 v176, v140
	v_mov_b32_e32 v142, v144
	v_mov_b32_e32 v143, v177
	v_pk_add_f32 v[140:141], v[140:141], v[144:145]
	v_pk_mul_f32 v[142:143], v[176:177], v[142:143]
	v_mul_f32_e32 v118, v173, v173
	v_mov_b32_e32 v141, v143
	v_pk_add_f32 v[142:143], v[182:183], v[182:183] op_sel:[0,1] op_sel_hi:[1,0]
	v_mov_b32_e32 v176, 0x358637bd
	v_mov_b32_e32 v143, v109
	v_pk_add_f32 v[140:141], v[140:141], v[142:143]
	v_pk_fma_f32 v[142:143], v[172:173], v[172:173], v[118:119] op_sel_hi:[1,1,0]
	v_mul_f32_e32 v118, v175, v175
	v_pk_fma_f32 v[144:145], v[174:175], v[174:175], v[118:119] op_sel_hi:[1,1,0]
	v_mov_b32_e32 v143, v120
	v_mov_b32_e32 v145, v155
	v_pk_add_f32 v[142:143], v[142:143], v[144:145]
	v_mov_b32_e32 v118, v1
	v_pk_add_f32 v[140:141], v[140:141], v[142:143]
	v_mov_b32_e32 v182, 0x3a800000
	v_add_f32_e32 v109, v140, v141
	v_pk_add_f32 v[126:127], v[112:113], 1.0 op_sel_hi:[1,0]
	v_pk_add_f32 v[112:113], v[158:159], 1.0 op_sel_hi:[1,0]
	v_add_f32_dpp v109, v109, v109 row_shr:1 row_mask:0xf bank_mask:0xf bound_ctrl:1
	v_pk_add_f32 v[144:145], v[156:157], 1.0 op_sel_hi:[1,0]
	s_waitcnt vmcnt(13)
; DI unsigned pk2(float lo, float hi) { f32x2 v = {lo, hi}; bf16x2v r = __builtin_convertvector(v, bf16x2v); return __builtin_bit_cast(unsigned, r); }
; DI void phase_n1(Frame& F, int l) {
;     ...
;         for (int rr = 0; rr < 2; ++rr) { const int r = blk * 16 + F.wave * 2 + rr;
;             f32x4 (&yv)[4] = yv2[rr]; f32x4 (&xv)[4] = xv2[rr];
;             const float rstd_y = rsqrtf(sumsq(yv, F.lane) * (1.0f / D) + RMS_EPS);
; #pragma unroll
;             for (int j = 0; j < 4; ++j) { const int o = 4 * F.lane + 256 * j; const f32x4 gv = gpm[j], gt = gtm[j];
;                 xv[j] = xv[j] + gt * (yv[j] * rstd_y * gv); u32x2 w; w.x = pk2(xv[j][0], xv[j][1]); w.y = pk2(xv[j][2], xv[j][3]); *(u32x2*)(xb + (size_t)r * D + o) = w; }
;             const float rstd_x = rsqrtf(sumsq(xv, F.lane) * (1.0f / D) + RMS_EPS);
;             mod_norm_store8(xv, rstd_x, mp, h8 + (size_t)r * D, F.lane, hv[rr]); }
	v_pk_add_f32 v[142:143], v[160:161], 1.0 op_sel_hi:[1,0]
	v_add_f32_dpp v109, v109, v109 row_shr:2 row_mask:0xf bank_mask:0xf bound_ctrl:1
	v_pk_add_f32 v[140:141], v[162:163], 1.0 op_sel_hi:[1,0]
	v_mov_b32_e32 v155, v1
	v_add_f32_dpp v109, v109, v109 row_shr:4 row_mask:0xf bank_mask:0xf bound_ctrl:1
	s_nop 1
	v_add_f32_dpp v109, v109, v109 row_shr:8 row_mask:0xf bank_mask:0xf bound_ctrl:1
	s_nop 1
	v_mov_b32_dpp v118, v109 row_bcast:15 row_mask:0xa bank_mask:0xf
	v_add_f32_e32 v109, v109, v118
	v_mov_b32_e32 v118, v1
	s_nop 1
	v_mov_b32_dpp v118, v109 row_bcast:31 row_mask:0xc bank_mask:0xf
	v_add_f32_e32 v109, v109, v118
	s_nop 0
	v_readlane_b32 s0, v109, 63
	s_nop 1
	v_fma_f32 v109, s0, v182, v176
	v_mul_f32_e32 v118, 0x4b800000, v109
	v_cmp_gt_f32_e32 vcc, s51, v109
	s_nop 1
	v_cndmask_b32_e32 v109, v109, v118, vcc
	v_rsq_f32_e32 v109, v109
	s_nop 0
	v_mul_f32_e32 v118, 0x45800000, v109
	v_cndmask_b32_e32 v118, v109, v118, vcc
	v_pk_mul_f32 v[156:157], v[118:119], v[166:167] op_sel_hi:[0,1]
	v_pk_mul_f32 v[158:159], v[118:119], v[164:165] op_sel_hi:[0,1]
	v_pk_mul_f32 v[158:159], v[70:71], v[158:159]
	v_pk_mul_f32 v[156:157], v[72:73], v[156:157]
	v_pk_fma_f32 v[62:63], v[74:75], v[158:159], v[62:63]
	v_pk_fma_f32 v[64:65], v[76:77], v[156:157], v[64:65]
	v_cvt_pk_bf16_f32 v156, v62, v63
	v_cvt_pk_bf16_f32 v157, v64, v65
	v_lshl_add_u64 v[158:159], v[100:101], 0, s[28:29]
	global_store_dwordx2 v[158:159], v[156:157], off nt
	v_mov_b32_e32 v156, v169
	v_mov_b32_e32 v157, v171
	v_mov_b32_e32 v169, v170
	v_pk_mul_f32 v[156:157], v[118:119], v[156:157] op_sel_hi:[0,1]
	v_pk_mul_f32 v[160:161], v[118:119], v[168:169] op_sel_hi:[0,1]
	v_pk_mul_f32 v[160:161], v[94:95], v[160:161]
	v_pk_mul_f32 v[156:157], v[96:97], v[156:157]
	s_waitcnt vmcnt(13)
	v_pk_fma_f32 v[58:59], v[90:91], v[160:161], v[58:59]
	v_pk_fma_f32 v[60:61], v[92:93], v[156:157], v[60:61]
	v_cvt_pk_bf16_f32 v156, v58, v59
	v_cvt_pk_bf16_f32 v157, v60, v61
	global_store_dwordx2 v[158:159], v[156:157], off offset:512 nt
	v_pk_mul_f32 v[156:157], v[118:119], v[174:175] op_sel_hi:[0,1]
	s_waitcnt vmcnt(10)
	v_pk_mul_f32 v[156:157], v[88:89], v[156:157]
	v_pk_mul_f32 v[162:163], v[118:119], v[178:179] op_sel_hi:[0,1]
	v_pk_fma_f32 v[156:157], v[84:85], v[156:157], v[52:53]
	v_pk_mul_f32 v[52:53], v[118:119], v[180:181] op_sel_hi:[0,1]
	s_waitcnt vmcnt(6)
	v_pk_mul_f32 v[162:163], v[78:79], v[162:163]
	v_pk_mul_f32 v[52:53], v[80:81], v[52:53]
	v_pk_fma_f32 v[162:163], v[66:67], v[162:163], v[38:39]
	v_pk_fma_f32 v[164:165], v[68:69], v[52:53], v[40:41]
	v_pk_mul_f32 v[38:39], v[64:65], v[64:65]
	v_pk_mul_f32 v[40:41], v[62:63], v[62:63]
	v_pk_mul_f32 v[160:161], v[118:119], v[172:173] op_sel_hi:[0,1]
	v_pk_mov_b32 v[52:53], v[40:41], v[38:39] op_sel:[1,0]
	v_mov_b32_e32 v41, v39
	v_pk_mul_f32 v[160:161], v[86:87], v[160:161]
	v_pk_add_f32 v[38:39], v[52:53], v[40:41]
	v_pk_fma_f32 v[160:161], v[82:83], v[160:161], v[50:51]
	v_pk_add_f32 v[38:39], v[38:39], v[38:39] op_sel_hi:[0,1]
	v_pk_mul_f32 v[40:41], v[60:61], v[60:61]
	v_pk_mul_f32 v[52:53], v[58:59], v[58:59]
	v_mul_f32_e32 v38, v160, v160
	v_pk_mov_b32 v[166:167], v[52:53], v[40:41] op_sel:[1,0]
	v_mov_b32_e32 v53, v41
	v_pk_add_f32 v[40:41], v[166:167], v[52:53]
	v_pk_fma_f32 v[52:53], v[160:161], v[160:161], v[38:39] op_sel_hi:[1,1,0]
	v_mul_f32_e32 v38, v156, v156
	v_pk_add_f32 v[40:41], v[40:41], v[40:41] op_sel_hi:[0,1]
	v_pk_fma_f32 v[166:167], v[156:157], v[156:157], v[38:39] op_sel_hi:[1,1,0]
	v_mul_f32_e32 v52, v162, v162
	v_mul_f32_e32 v166, v163, v163
	v_mul_f32_e32 v38, v164, v164
	v_mul_f32_e32 v40, v165, v165
	v_pk_add_f32 v[52:53], v[52:53], v[166:167]
	v_pk_add_f32 v[38:39], v[38:39], v[40:41]
	v_cvt_pk_bf16_f32 v50, v160, v161
	v_pk_add_f32 v[38:39], v[52:53], v[38:39]
	v_cvt_pk_bf16_f32 v51, v156, v157
	v_add_f32_e32 v38, v38, v39
	v_mov_b32_e32 v39, v1
	global_store_dwordx2 v[158:159], v[50:51], off offset:1024 nt
	v_add_f32_dpp v38, v38, v38 row_shr:1 row_mask:0xf bank_mask:0xf bound_ctrl:1
	v_cvt_pk_bf16_f32 v50, v162, v163
	v_mov_b32_e32 v109, v1
	v_add_f32_dpp v38, v38, v38 row_shr:2 row_mask:0xf bank_mask:0xf bound_ctrl:1
	v_mov_b32_e32 v166, v1
	v_mul_f32_e32 v167, v119, v119
	v_add_f32_dpp v38, v38, v38 row_shr:4 row_mask:0xf bank_mask:0xf bound_ctrl:1
	v_mul_f32_e32 v168, v122, v122
	v_mul_f32_e32 v169, v123, v123
	v_add_f32_dpp v38, v38, v38 row_shr:8 row_mask:0xf bank_mask:0xf bound_ctrl:1
	s_nop 1
	v_mov_b32_dpp v39, v38 row_bcast:15 row_mask:0xa bank_mask:0xf
	v_add_f32_e32 v38, v38, v39
	v_mov_b32_e32 v39, v1
	s_nop 1
	v_mov_b32_dpp v39, v38 row_bcast:31 row_mask:0xc bank_mask:0xf
	v_add_f32_e32 v38, v38, v39
	s_nop 0
	v_readlane_b32 s0, v38, 63
	s_nop 1
	v_fma_f32 v38, s0, v182, v176
	v_mul_f32_e32 v39, 0x4b800000, v38
	v_cmp_gt_f32_e32 vcc, s51, v38
	s_nop 1
	v_cndmask_b32_e32 v38, v38, v39, vcc
	v_rsq_f32_e32 v38, v38
	s_nop 0
	v_mul_f32_e32 v39, 0x45800000, v38
	v_cndmask_b32_e32 v118, v38, v39, vcc
	v_pk_mul_f32 v[40:41], v[62:63], v[118:119] op_sel_hi:[1,0]
	v_pk_mul_f32 v[38:39], v[64:65], v[118:119] op_sel_hi:[1,0]
	s_waitcnt vmcnt(6)
	v_pk_mul_f32 v[40:41], v[54:55], v[40:41]
	v_mov_b32_e32 v62, v1
	v_pk_fma_f32 v[40:41], v[126:127], v[40:41], v[46:47]
	v_pk_mul_f32 v[38:39], v[56:57], v[38:39]
	v_mul_f32_e32 v51, 0x41800000, v40
	v_mul_f32_e32 v52, 0x41800000, v41
	v_med3_f32 v51, v51, s53, v204
	v_med3_f32 v52, v52, s53, v204
	v_cvt_pk_fp8_f32 v62, v51, v52
	v_pk_fma_f32 v[38:39], v[124:125], v[38:39], v[48:49]
	s_nop 0
	v_mul_f32_e32 v53, 0x41800000, v38
	v_mul_f32_e32 v51, 0x41800000, v39
	v_med3_f32 v52, v53, s53, v204
	v_med3_f32 v51, v51, s53, v204
	v_cvt_pk_fp8_f32 v62, v52, v51 op_sel:[0,0,1]
	v_pk_mul_f32 v[52:53], v[58:59], v[118:119] op_sel_hi:[1,0]
	v_cvt_pk_bf16_f32 v51, v164, v165
	s_waitcnt vmcnt(5)
; DI unsigned pk2(float lo, float hi) { f32x2 v = {lo, hi}; bf16x2v r = __builtin_convertvector(v, bf16x2v); return __builtin_bit_cast(unsigned, r); }
; DI unsigned pk4_fp8(float a, float b, float c, float d) { int r = 0; r = __builtin_amdgcn_cvt_pk_fp8_f32(sat8(a), sat8(b), r, false); r = __builtin_amdgcn_cvt_pk_fp8_f32(sat8(c), sat8(d), r, true); return (unsigned)r; }
; DI void mod_norm_store8(const f32x4 (&xv)[4], float rstd, const ModP& m, unsigned char* orow, int lane, f32x4 (&hv)[4]) {
; #pragma unroll
;     ...
;         hv[j] = xv[j] * rstd * gv * (1.0f + scv) + shv;
;         *(unsigned*)(orow + o) = pk4_fp8(hv[j][0] * H8_SCALE, hv[j][1] * H8_SCALE, hv[j][2] * H8_SCALE, hv[j][3] * H8_SCALE); }
; }
; DI void phase_n1(Frame& F, int l) {
;     ...
;         for (int rr = 0; rr < 2; ++rr) { const int r = blk * 16 + F.wave * 2 + rr;
;             f32x4 (&yv)[4] = yv2[rr]; f32x4 (&xv)[4] = xv2[rr];
;             const float rstd_y = rsqrtf(sumsq(yv, F.lane) * (1.0f / D) + RMS_EPS);
; #pragma unroll
;             for (int j = 0; j < 4; ++j) { const int o = 4 * F.lane + 256 * j; const f32x4 gv = gpm[j], gt = gtm[j];
;                 xv[j] = xv[j] + gt * (yv[j] * rstd_y * gv); u32x2 w; w.x = pk2(xv[j][0], xv[j][1]); w.y = pk2(xv[j][2], xv[j][3]); *(u32x2*)(xb + (size_t)r * D + o) = w; }
;             const float rstd_x = rsqrtf(sumsq(xv, F.lane) * (1.0f / D) + RMS_EPS);
;             mod_norm_store8(xv, rstd_x, mp, h8 + (size_t)r * D, F.lane, hv[rr]); }
	v_pk_mul_f32 v[52:53], v[42:43], v[52:53]
	global_store_dwordx2 v[158:159], v[50:51], off offset:1536 nt
	v_pk_fma_f32 v[52:53], v[116:117], v[52:53], v[34:35]
	v_pk_mul_f32 v[50:51], v[60:61], v[118:119] op_sel_hi:[1,0]
	v_mul_f32_e32 v58, 0x41800000, v52
	v_mul_f32_e32 v59, 0x41800000, v53
	v_pk_mul_f32 v[50:51], v[44:45], v[50:51]
	v_med3_f32 v58, v58, s53, v204
	v_med3_f32 v59, v59, s53, v204
	v_pk_fma_f32 v[50:51], v[114:115], v[50:51], v[36:37]
	v_cvt_pk_fp8_f32 v109, v58, v59
	v_mul_f32_e32 v60, 0x41800000, v50
	v_mul_f32_e32 v58, 0x41800000, v51
	v_med3_f32 v59, v60, s53, v204
	v_pk_mul_f32 v[60:61], v[160:161], v[118:119] op_sel_hi:[1,0]
	v_med3_f32 v58, v58, s53, v204
	s_waitcnt vmcnt(5)
	v_pk_mul_f32 v[60:61], v[30:31], v[60:61]
	v_lshl_add_u64 v[158:159], v[104:105], 0, s[26:27]
	v_cvt_pk_fp8_f32 v109, v59, v58 op_sel:[0,0,1]
	v_pk_mul_f32 v[58:59], v[156:157], v[118:119] op_sel_hi:[1,0]
	v_pk_fma_f32 v[60:61], v[144:145], v[60:61], v[26:27]
	global_store_dword v[158:159], v62, off
	v_pk_mul_f32 v[58:59], v[32:33], v[58:59]
	v_mul_f32_e32 v62, 0x41800000, v60
	v_mul_f32_e32 v63, 0x41800000, v61
	v_pk_fma_f32 v[58:59], v[112:113], v[58:59], v[28:29]
	v_med3_f32 v62, v62, s53, v204
	v_med3_f32 v63, v63, s53, v204
	v_mul_f32_e32 v64, 0x41800000, v58
	v_cvt_pk_fp8_f32 v155, v62, v63
	v_med3_f32 v63, v64, s53, v204
	v_pk_mul_f32 v[64:65], v[162:163], v[118:119] op_sel_hi:[1,0]
	v_mul_f32_e32 v62, 0x41800000, v59
	s_waitcnt vmcnt(5)
	v_pk_mul_f32 v[64:65], v[22:23], v[64:65]
	v_med3_f32 v62, v62, s53, v204
	v_pk_fma_f32 v[64:65], v[142:143], v[64:65], v[18:19]
	v_cvt_pk_fp8_f32 v155, v63, v62 op_sel:[0,0,1]
	v_pk_mul_f32 v[62:63], v[164:165], v[118:119] op_sel_hi:[1,0]
	v_mul_f32_e32 v118, 0x41800000, v64
	v_mul_f32_e32 v120, 0x41800000, v65
	v_med3_f32 v118, v118, s53, v204
	v_med3_f32 v120, v120, s53, v204
	v_pk_mul_f32 v[62:63], v[24:25], v[62:63]
	v_cvt_pk_fp8_f32 v166, v118, v120
	v_pk_fma_f32 v[62:63], v[140:141], v[62:63], v[20:21]
	v_pk_mul_f32 v[160:161], v[134:135], v[134:135]
	v_mul_f32_e32 v156, 0x41800000, v62
	v_mul_f32_e32 v118, 0x41800000, v63
	v_med3_f32 v120, v156, s53, v204
	v_med3_f32 v118, v118, s53, v204
	v_cvt_pk_fp8_f32 v166, v120, v118 op_sel:[0,0,1]
	v_mul_f32_e32 v118, v139, v139
	v_pk_fma_f32 v[156:157], v[138:139], v[138:139], v[118:119] op_sel_hi:[1,1,0]
	v_mul_f32_e32 v118, v137, v137
	v_pk_fma_f32 v[162:163], v[136:137], v[136:137], v[118:119] op_sel_hi:[1,1,0]
	v_pk_fma_f32 v[160:161], v[132:133], v[132:133], v[160:161]
	v_mov_b32_e32 v120, v162
	v_mov_b32_e32 v164, v156
	v_mov_b32_e32 v165, v121
	v_pk_add_f32 v[156:157], v[162:163], v[156:157]
	v_pk_mul_f32 v[162:163], v[120:121], v[164:165]
	v_pk_add_f32 v[160:161], v[160:161], v[160:161] op_sel:[0,1] op_sel_hi:[1,0]
	v_mov_b32_e32 v157, v163
	v_mov_b32_e32 v161, v167
	v_mul_f32_e32 v118, v129, v129
	v_pk_add_f32 v[156:157], v[156:157], v[160:161]
	v_pk_fma_f32 v[160:161], v[128:129], v[128:129], v[118:119] op_sel_hi:[1,1,0]
	v_mul_f32_e32 v118, v131, v131
	v_pk_fma_f32 v[162:163], v[130:131], v[130:131], v[118:119] op_sel_hi:[1,1,0]
	v_mov_b32_e32 v161, v168
	v_mov_b32_e32 v163, v169
	v_pk_add_f32 v[160:161], v[160:161], v[162:163]
	v_mov_b32_e32 v120, v1
	v_pk_add_f32 v[156:157], v[156:157], v[160:161]
	global_store_dword v[158:159], v109, off offset:256
	global_store_dword v[158:159], v155, off offset:512
	global_store_dword v[158:159], v166, off offset:768
	v_add_f32_e32 v118, v156, v157
	s_nop 1
	v_add_f32_dpp v118, v118, v118 row_shr:1 row_mask:0xf bank_mask:0xf bound_ctrl:1
	s_nop 1
	v_add_f32_dpp v118, v118, v118 row_shr:2 row_mask:0xf bank_mask:0xf bound_ctrl:1
	s_nop 1
	v_add_f32_dpp v118, v118, v118 row_shr:4 row_mask:0xf bank_mask:0xf bound_ctrl:1
	s_nop 1
	v_add_f32_dpp v118, v118, v118 row_shr:8 row_mask:0xf bank_mask:0xf bound_ctrl:1
	s_nop 1
	v_mov_b32_dpp v120, v118 row_bcast:15 row_mask:0xa bank_mask:0xf
	v_add_f32_e32 v118, v118, v120
	v_mov_b32_e32 v120, v1
	s_nop 1
	v_mov_b32_dpp v120, v118 row_bcast:31 row_mask:0xc bank_mask:0xf
	v_add_f32_e32 v118, v118, v120
	s_nop 0
	v_readlane_b32 s0, v118, 63
	s_nop 1
	v_fma_f32 v118, s0, v182, v176
	v_mul_f32_e32 v120, 0x4b800000, v118
	v_cmp_gt_f32_e32 vcc, s51, v118
	s_nop 1
	v_cndmask_b32_e32 v118, v118, v120, vcc
	v_rsq_f32_e32 v118, v118
	s_nop 0
	v_mul_f32_e32 v109, 0x45800000, v118
	v_cndmask_b32_e32 v120, v118, v109, vcc
	v_pk_mul_f32 v[138:139], v[120:121], v[138:139] op_sel_hi:[0,1]
	v_pk_mul_f32 v[136:137], v[120:121], v[136:137] op_sel_hi:[0,1]
	v_pk_mul_f32 v[70:71], v[70:71], v[136:137]
	v_pk_mul_f32 v[72:73], v[72:73], v[138:139]
	v_pk_fma_f32 v[14:15], v[74:75], v[70:71], v[14:15]
	v_pk_fma_f32 v[16:17], v[76:77], v[72:73], v[16:17]
	v_cvt_pk_bf16_f32 v70, v14, v15
	v_cvt_pk_bf16_f32 v71, v16, v17
	v_lshl_add_u64 v[72:73], v[100:101], 0, s[14:15]
	global_store_dwordx2 v[72:73], v[70:71], off nt
	v_mov_b32_e32 v70, v133
	v_mov_b32_e32 v71, v135
	v_mov_b32_e32 v133, v134
	v_pk_mul_f32 v[70:71], v[120:121], v[70:71] op_sel_hi:[0,1]
	v_pk_mul_f32 v[74:75], v[120:121], v[132:133] op_sel_hi:[0,1]
	v_pk_mul_f32 v[74:75], v[94:95], v[74:75]
	v_pk_mul_f32 v[70:71], v[96:97], v[70:71]
	v_pk_fma_f32 v[10:11], v[90:91], v[74:75], v[10:11]
	v_pk_fma_f32 v[12:13], v[92:93], v[70:71], v[12:13]
	v_cvt_pk_bf16_f32 v70, v10, v11
	v_cvt_pk_bf16_f32 v71, v12, v13
	global_store_dwordx2 v[72:73], v[70:71], off offset:512 nt
	v_pk_mul_f32 v[70:71], v[120:121], v[130:131] op_sel_hi:[0,1]
	v_pk_mul_f32 v[74:75], v[120:121], v[128:129] op_sel_hi:[0,1]
	v_pk_mul_f32 v[74:75], v[86:87], v[74:75]
	v_pk_mul_f32 v[70:71], v[88:89], v[70:71]
	v_pk_fma_f32 v[6:7], v[82:83], v[74:75], v[6:7]
; #define LAS __attribute__((address_space(3)))
; DI unsigned pk2(float lo, float hi) { f32x2 v = {lo, hi}; bf16x2v r = __builtin_convertvector(v, bf16x2v); return __builtin_bit_cast(unsigned, r); }
; DI void phase_n1(Frame& F, int l) {
;     ...
;         for (int rr = 0; rr < 2; ++rr) { const int r = blk * 16 + F.wave * 2 + rr;
;             f32x4 (&yv)[4] = yv2[rr]; f32x4 (&xv)[4] = xv2[rr];
;             const float rstd_y = rsqrtf(sumsq(yv, F.lane) * (1.0f / D) + RMS_EPS);
; #pragma unroll
;             for (int j = 0; j < 4; ++j) { const int o = 4 * F.lane + 256 * j; const f32x4 gv = gpm[j], gt = gtm[j];
;                 xv[j] = xv[j] + gt * (yv[j] * rstd_y * gv); u32x2 w; w.x = pk2(xv[j][0], xv[j][1]); w.y = pk2(xv[j][2], xv[j][3]); *(u32x2*)(xb + (size_t)r * D + o) = w; }
;             const float rstd_x = rsqrtf(sumsq(xv, F.lane) * (1.0f / D) + RMS_EPS);
;             mod_norm_store8(xv, rstd_x, mp, h8 + (size_t)r * D, F.lane, hv[rr]); }
; #pragma unroll
;         for (int rr = 0; rr < 2; ++rr)
; #pragma unroll
;             for (int j = 0; j < 4; ++j) { u32x2 w; w.x = pk2(hv[rr][j][0], hv[rr][j][1]); w.y = pk2(hv[rr][j][2], hv[rr][j][3]); *(LAS u32x2*)(HTl + (F.wave * 2 + rr) * RP + (4 * F.lane + 256 * j) * 2) = w; }
;         __syncthreads();
	v_pk_fma_f32 v[8:9], v[84:85], v[70:71], v[8:9]
	v_cvt_pk_bf16_f32 v70, v6, v7
	v_cvt_pk_bf16_f32 v71, v8, v9
	v_mov_b32_e32 v118, v121
	global_store_dwordx2 v[72:73], v[70:71], off offset:1024 nt
	v_pk_mul_f32 v[70:71], v[120:121], v[122:123] op_sel_hi:[0,1]
	v_pk_mul_f32 v[74:75], v[120:121], v[118:119] op_sel_hi:[0,1]
	v_pk_mul_f32 v[74:75], v[78:79], v[74:75]
	v_pk_mul_f32 v[70:71], v[80:81], v[70:71]
	v_pk_fma_f32 v[2:3], v[66:67], v[74:75], v[2:3]
	v_pk_fma_f32 v[4:5], v[68:69], v[70:71], v[4:5]
	v_pk_mul_f32 v[66:67], v[16:17], v[16:17]
	v_pk_mul_f32 v[68:69], v[14:15], v[14:15]
	s_nop 0
	v_pk_mov_b32 v[70:71], v[68:69], v[66:67] op_sel:[1,0]
	v_mov_b32_e32 v69, v67
	v_pk_add_f32 v[66:67], v[70:71], v[68:69]
	v_pk_mul_f32 v[68:69], v[12:13], v[12:13]
	v_pk_add_f32 v[66:67], v[66:67], v[66:67] op_sel_hi:[0,1]
	v_pk_mul_f32 v[70:71], v[10:11], v[10:11]
	v_mul_f32_e32 v66, v6, v6
	v_pk_mov_b32 v[74:75], v[70:71], v[68:69] op_sel:[1,0]
	v_mov_b32_e32 v71, v69
	v_pk_add_f32 v[68:69], v[74:75], v[70:71]
	v_pk_fma_f32 v[70:71], v[6:7], v[6:7], v[66:67] op_sel_hi:[1,1,0]
	v_mul_f32_e32 v66, v8, v8
	v_pk_add_f32 v[68:69], v[68:69], v[68:69] op_sel_hi:[0,1]
	v_pk_fma_f32 v[74:75], v[8:9], v[8:9], v[66:67] op_sel_hi:[1,1,0]
	v_mul_f32_e32 v70, v2, v2
	v_mul_f32_e32 v74, v3, v3
	v_mul_f32_e32 v66, v4, v4
	v_mul_f32_e32 v68, v5, v5
	v_pk_add_f32 v[70:71], v[70:71], v[74:75]
	v_pk_add_f32 v[66:67], v[66:67], v[68:69]
	s_nop 0
	v_pk_add_f32 v[66:67], v[70:71], v[66:67]
	s_nop 0
	v_add_f32_e32 v66, v66, v67
	v_mov_b32_e32 v67, v1
	s_nop 0
	v_add_f32_dpp v66, v66, v66 row_shr:1 row_mask:0xf bank_mask:0xf bound_ctrl:1
	s_nop 1
	v_add_f32_dpp v66, v66, v66 row_shr:2 row_mask:0xf bank_mask:0xf bound_ctrl:1
	s_nop 1
	v_add_f32_dpp v66, v66, v66 row_shr:4 row_mask:0xf bank_mask:0xf bound_ctrl:1
	s_nop 1
	v_add_f32_dpp v66, v66, v66 row_shr:8 row_mask:0xf bank_mask:0xf bound_ctrl:1
	s_nop 1
	v_mov_b32_dpp v67, v66 row_bcast:15 row_mask:0xa bank_mask:0xf
	v_add_f32_e32 v66, v66, v67
	v_mov_b32_e32 v67, v1
	s_nop 1
	v_mov_b32_dpp v67, v66 row_bcast:31 row_mask:0xc bank_mask:0xf
	v_add_f32_e32 v66, v66, v67
	s_nop 0
	v_readlane_b32 s0, v66, 63
	s_nop 1
	v_fma_f32 v66, s0, v182, v176
	v_mul_f32_e32 v67, 0x4b800000, v66
	v_cmp_gt_f32_e32 vcc, s51, v66
	s_nop 1
	v_cndmask_b32_e32 v66, v66, v67, vcc
	v_rsq_f32_e32 v68, v66
	v_cvt_pk_bf16_f32 v66, v2, v3
	v_cvt_pk_bf16_f32 v67, v4, v5
	global_store_dwordx2 v[72:73], v[66:67], off offset:1536 nt
	v_mul_f32_e32 v66, 0x45800000, v68
	v_cndmask_b32_e32 v66, v68, v66, vcc
	v_pk_mul_f32 v[14:15], v[14:15], v[66:67] op_sel_hi:[1,0]
	v_pk_mul_f32 v[10:11], v[10:11], v[66:67] op_sel_hi:[1,0]
	v_pk_mul_f32 v[14:15], v[54:55], v[14:15]
	v_pk_mul_f32 v[16:17], v[16:17], v[66:67] op_sel_hi:[1,0]
	v_pk_fma_f32 v[14:15], v[126:127], v[14:15], v[46:47]
	v_pk_mul_f32 v[10:11], v[42:43], v[10:11]
	v_pk_mul_f32 v[6:7], v[6:7], v[66:67] op_sel_hi:[1,0]
	v_pk_mul_f32 v[16:17], v[56:57], v[16:17]
	v_mul_f32_e32 v46, 0x41800000, v14
	v_mul_f32_e32 v47, 0x41800000, v15
	v_pk_mul_f32 v[12:13], v[12:13], v[66:67] op_sel_hi:[1,0]
	v_pk_fma_f32 v[10:11], v[116:117], v[10:11], v[34:35]
	v_pk_mul_f32 v[6:7], v[30:31], v[6:7]
	v_pk_mul_f32 v[2:3], v[2:3], v[66:67] op_sel_hi:[1,0]
	v_pk_fma_f32 v[16:17], v[124:125], v[16:17], v[48:49]
	v_med3_f32 v46, v46, s53, v204
	v_med3_f32 v47, v47, s53, v204
	v_mov_b32_e32 v49, v1
	v_pk_mul_f32 v[12:13], v[44:45], v[12:13]
	v_mul_f32_e32 v34, 0x41800000, v10
	v_mul_f32_e32 v35, 0x41800000, v11
	v_pk_mul_f32 v[8:9], v[8:9], v[66:67] op_sel_hi:[1,0]
	v_pk_fma_f32 v[6:7], v[144:145], v[6:7], v[26:27]
	v_pk_mul_f32 v[2:3], v[22:23], v[2:3]
	v_cvt_pk_fp8_f32 v49, v46, v47
	v_pk_fma_f32 v[12:13], v[114:115], v[12:13], v[36:37]
	v_med3_f32 v34, v34, s53, v204
	v_med3_f32 v35, v35, s53, v204
	v_mov_b32_e32 v37, v1
	v_pk_mul_f32 v[8:9], v[32:33], v[8:9]
	v_mul_f32_e32 v26, 0x41800000, v6
	v_mul_f32_e32 v27, 0x41800000, v7
	v_pk_mul_f32 v[4:5], v[4:5], v[66:67] op_sel_hi:[1,0]
	v_pk_fma_f32 v[2:3], v[142:143], v[2:3], v[18:19]
	v_cvt_pk_fp8_f32 v37, v34, v35
	v_pk_fma_f32 v[8:9], v[112:113], v[8:9], v[28:29]
	v_med3_f32 v26, v26, s53, v204
	v_med3_f32 v27, v27, s53, v204
	v_mov_b32_e32 v29, v1
	v_pk_mul_f32 v[4:5], v[24:25], v[4:5]
	v_mul_f32_e32 v18, 0x41800000, v2
	v_mul_f32_e32 v19, 0x41800000, v3
	v_mul_f32_e32 v48, 0x41800000, v16
	v_mul_f32_e32 v46, 0x41800000, v17
	v_cvt_pk_fp8_f32 v29, v26, v27
	v_pk_fma_f32 v[4:5], v[140:141], v[4:5], v[20:21]
	v_med3_f32 v18, v18, s53, v204
	v_med3_f32 v19, v19, s53, v204
	v_mov_b32_e32 v21, v1
	v_med3_f32 v47, v48, s53, v204
	v_med3_f32 v46, v46, s53, v204
	v_mul_f32_e32 v36, 0x41800000, v12
	v_mul_f32_e32 v34, 0x41800000, v13
	v_cvt_pk_fp8_f32 v21, v18, v19
	v_cvt_pk_fp8_f32 v49, v47, v46 op_sel:[0,0,1]
	v_med3_f32 v35, v36, s53, v204
	v_med3_f32 v34, v34, s53, v204
	v_mul_f32_e32 v28, 0x41800000, v8
	v_mul_f32_e32 v26, 0x41800000, v9
	v_cvt_pk_fp8_f32 v37, v35, v34 op_sel:[0,0,1]
	v_med3_f32 v27, v28, s53, v204
	v_med3_f32 v26, v26, s53, v204
	v_mul_f32_e32 v20, 0x41800000, v4
	v_mul_f32_e32 v18, 0x41800000, v5
	v_cvt_pk_fp8_f32 v29, v27, v26 op_sel:[0,0,1]
	v_med3_f32 v19, v20, s53, v204
	v_med3_f32 v18, v18, s53, v204
	v_lshl_add_u64 v[46:47], v[104:105], 0, s[2:3]
	v_cvt_pk_fp8_f32 v21, v19, v18 op_sel:[0,0,1]
	global_store_dword v[46:47], v49, off
	global_store_dword v[46:47], v37, off offset:256
	global_store_dword v[46:47], v29, off offset:512
	global_store_dword v[46:47], v21, off offset:768
	v_cvt_pk_bf16_f32 v18, v40, v41
	v_cvt_pk_bf16_f32 v19, v38, v39
	v_cvt_pk_bf16_f32 v20, v52, v53
	v_cvt_pk_bf16_f32 v21, v50, v51
	ds_write2st64_b64 v150, v[18:19], v[20:21] offset1:1
	v_cvt_pk_bf16_f32 v18, v60, v61
	v_cvt_pk_bf16_f32 v19, v58, v59
	v_cvt_pk_bf16_f32 v20, v64, v65
	v_cvt_pk_bf16_f32 v21, v62, v63
	v_cvt_pk_bf16_f32 v14, v14, v15
	v_cvt_pk_bf16_f32 v15, v16, v17
	v_cvt_pk_bf16_f32 v10, v10, v11
	v_cvt_pk_bf16_f32 v11, v12, v13
	v_add_u32_e32 v12, 16, v150
	v_cvt_pk_bf16_f32 v6, v6, v7
	v_cvt_pk_bf16_f32 v7, v8, v9
	v_cvt_pk_bf16_f32 v2, v2, v3
	v_cvt_pk_bf16_f32 v3, v4, v5
	ds_write2st64_b64 v150, v[18:19], v[20:21] offset0:2 offset1:3
	ds_write2st64_b64 v12, v[14:15], v[10:11] offset0:4 offset1:5
	ds_write2st64_b64 v12, v[6:7], v[2:3] offset0:6 offset1:7
	s_waitcnt lgkmcnt(0)
	s_barrier
; #define LAS __attribute__((address_space(3)))
; DI void phase_n1(Frame& F, int l) {
;     ...
;         { const int r16 = F.lane & 15, kg = F.lane >> 4; f32x4 c0 = (f32x4){0.f, 0.f, 0.f, 0.f}, c1 = c0;
; #pragma unroll
;           for (int st = 0; st < 4; ++st) { const int kb2 = (128 * F.wave + 32 * st + 8 * kg) * 2;
;               const bf16x8 af = *(const LAS bf16x8*)(HTl + r16 * RP + kb2), b0 = *(const LAS bf16x8*)(WTl + r16 * RP + kb2), b1 = *(const LAS bf16x8*)(WTl + (16 + r16) * RP + kb2);
;               c0 = __builtin_amdgcn_mfma_f32_16x16x32_bf16(af, b0, c0, 0, 0, 0); c1 = __builtin_amdgcn_mfma_f32_16x16x32_bf16(af, b1, c1, 0, 0, 0); }
; #pragma unroll
;           for (int i = 0; i < 4; ++i) { PS[(F.wave * 16 + 4 * kg + i) * 32 + r16] = c0[i]; PS[(F.wave * 16 + 4 * kg + i) * 32 + 16 + r16] = c1[i]; } }
;         __syncthreads();
;         float lgs = 0.f;
; #pragma unroll
;         for (int w = 0; w < 8; ++w) lgs += PS[(w * 16 + F.wave * 2 + (F.lane >> 5)) * 32 + (F.lane & 31)];
;         float lg = lgs + brt; const int e_me = F.lane & 31;
;         float topv[4]; int tope[4];
; #pragma unroll
;         for (int k = 0; k < 4; ++k) { float mv = lg; int mi = e_me;
; #pragma unroll
;             for (int st = 0; st < 4; ++st) {
;                 float ov; int oi;
;                 if (st == 0) { ov = __int_as_float(__builtin_amdgcn_update_dpp(0, __float_as_int(mv), 0x121, 0xf, 0xf, false)); oi = __builtin_amdgcn_update_dpp(0, mi, 0x121, 0xf, 0xf, false); }
;                 else if (st == 1) { ov = __int_as_float(__builtin_amdgcn_update_dpp(0, __float_as_int(mv), 0x122, 0xf, 0xf, false)); oi = __builtin_amdgcn_update_dpp(0, mi, 0x122, 0xf, 0xf, false); }
;                 else if (st == 2) { ov = __int_as_float(__builtin_amdgcn_update_dpp(0, __float_as_int(mv), 0x124, 0xf, 0xf, false)); oi = __builtin_amdgcn_update_dpp(0, mi, 0x124, 0xf, 0xf, false); }
;                 else { ov = __int_as_float(__builtin_amdgcn_update_dpp(0, __float_as_int(mv), 0x128, 0xf, 0xf, false)); oi = __builtin_amdgcn_update_dpp(0, mi, 0x128, 0xf, 0xf, false); }
;                 if (ov > mv || (ov == mv && oi < mi)) { mv = ov; mi = oi; } }
;             { const float ov = shx(mv, 16, F.lane); const int oi = shxi(mi, 16, F.lane); if (ov > mv || (ov == mv && oi < mi)) { mv = ov; mi = oi; } }
	ds_read_b128 v[2:5], v151
	ds_read_b128 v[6:9], v152
	ds_read_b128 v[10:13], v151 offset:64
	ds_read_b128 v[14:17], v152 offset:64
	s_waitcnt lgkmcnt(2)
	v_mfma_f32_16x16x32_bf16 v[6:9], v[2:5], v[6:9], 0
	ds_read_b128 v[18:21], v152 offset:33024
	ds_read_b128 v[22:25], v152 offset:33088
	s_waitcnt lgkmcnt(2)
	v_mfma_f32_16x16x32_bf16 v[6:9], v[10:13], v[14:17], v[6:9]
	ds_read_b128 v[14:17], v151 offset:128
	s_waitcnt lgkmcnt(2)
	v_mfma_f32_16x16x32_bf16 v[2:5], v[2:5], v[18:21], 0
	s_waitcnt lgkmcnt(1)
	v_mfma_f32_16x16x32_bf16 v[2:5], v[10:13], v[22:25], v[2:5]
	ds_read_b128 v[10:13], v152 offset:128
	ds_read_b128 v[18:21], v151 offset:192
	ds_read_b128 v[22:25], v152 offset:192
	s_waitcnt lgkmcnt(2)
	v_mfma_f32_16x16x32_bf16 v[6:9], v[14:17], v[10:13], v[6:9]
	ds_read_b128 v[10:13], v152 offset:33152
	ds_read_b128 v[26:29], v152 offset:33216
	s_waitcnt lgkmcnt(1)
	v_mfma_f32_16x16x32_bf16 v[2:5], v[14:17], v[10:13], v[2:5]
	v_mfma_f32_16x16x32_bf16 v[6:9], v[18:21], v[22:25], v[6:9]
	s_waitcnt lgkmcnt(0)
	v_mfma_f32_16x16x32_bf16 v[2:5], v[18:21], v[26:29], v[2:5]
	s_nop 7
	ds_write2_b32 v153, v6, v2 offset1:16
	ds_write2_b32 v153, v7, v3 offset0:32 offset1:48
	ds_write2_b32 v153, v8, v4 offset0:64 offset1:80
	ds_write2_b32 v153, v9, v5 offset0:96 offset1:112
	s_waitcnt lgkmcnt(0)
	s_barrier
	ds_read2st64_b32 v[2:3], v154 offset1:8
	ds_read2st64_b32 v[4:5], v154 offset0:16 offset1:24
	ds_read2st64_b32 v[6:7], v154 offset0:32 offset1:40
	s_waitcnt lgkmcnt(2)
	v_add_f32_e32 v2, 0, v2
	v_add_f32_e32 v8, v2, v3
	ds_read2st64_b32 v[2:3], v154 offset0:48 offset1:56
	s_waitcnt lgkmcnt(2)
	v_add_f32_e32 v4, v8, v4
	v_add_f32_e32 v4, v4, v5
	s_waitcnt lgkmcnt(1)
	v_add_f32_e32 v4, v4, v6
	v_add_f32_e32 v4, v4, v7
	s_waitcnt lgkmcnt(0)
	v_add_f32_e32 v2, v4, v2
	v_add_f32_e32 v2, v2, v3
	v_add_f32_e32 v4, v0, v2
	v_mov_b32_e32 v6, v1
	v_mov_b32_e32 v7, v1
	s_nop 0
	v_mov_b32_dpp v6, v4 row_ror:1 row_mask:0xf bank_mask:0xf
	v_mov_b32_dpp v7, v146 row_ror:1 row_mask:0xf bank_mask:0xf
	v_cmp_lt_f32_e64 s[2:3], v4, v6
	v_cmp_nlt_f32_e32 vcc, v4, v6
	s_and_saveexec_b64 s[16:17], vcc
	v_cmp_eq_f32_e32 vcc, v4, v6
	v_cmp_lt_i32_e64 s[14:15], v7, v146
	s_and_b64 s[0:1], vcc, s[14:15]
	s_andn2_b64 s[2:3], s[2:3], exec
	s_and_b64 s[0:1], s[0:1], exec
	s_or_b64 s[2:3], s[2:3], s[0:1]
	s_or_b64 exec, exec, s[16:17]
	v_mov_b32_e32 v5, v4
	v_mov_b32_e32 v3, v4
	v_mov_b32_e32 v2, v146
	s_and_saveexec_b64 s[14:15], s[2:3]
	v_mov_b32_e32 v5, v6
	v_mov_b32_e32 v3, v6
	v_mov_b32_e32 v2, v7
	s_or_b64 exec, exec, s[14:15]
	v_mov_b32_e32 v6, v1
	v_mov_b32_e32 v7, v1
	s_nop 0
	v_mov_b32_dpp v6, v5 row_ror:2 row_mask:0xf bank_mask:0xf
	v_mov_b32_dpp v7, v2 row_ror:2 row_mask:0xf bank_mask:0xf
	v_cmp_lt_f32_e64 s[2:3], v3, v6
	v_cmp_nlt_f32_e32 vcc, v3, v6
	s_and_saveexec_b64 s[16:17], vcc
	v_cmp_eq_f32_e32 vcc, v3, v6
	v_cmp_lt_i32_e64 s[14:15], v7, v2
	s_and_b64 s[0:1], vcc, s[14:15]
	s_andn2_b64 s[2:3], s[2:3], exec
	s_and_b64 s[0:1], s[0:1], exec
	s_or_b64 s[2:3], s[2:3], s[0:1]
	s_or_b64 exec, exec, s[16:17]
	s_and_saveexec_b64 s[14:15], s[2:3]
	v_mov_b32_e32 v5, v6
	v_mov_b32_e32 v3, v6
	v_mov_b32_e32 v2, v7
	s_or_b64 exec, exec, s[14:15]
	v_mov_b32_e32 v6, v1
	v_mov_b32_e32 v7, v1
	s_nop 0
	v_mov_b32_dpp v6, v5 row_ror:4 row_mask:0xf bank_mask:0xf
	v_mov_b32_dpp v7, v2 row_ror:4 row_mask:0xf bank_mask:0xf
	v_cmp_lt_f32_e64 s[2:3], v3, v6
	v_cmp_nlt_f32_e32 vcc, v3, v6
	s_and_saveexec_b64 s[16:17], vcc
	v_cmp_eq_f32_e32 vcc, v3, v6
	v_cmp_lt_i32_e64 s[14:15], v7, v2
	s_and_b64 s[0:1], vcc, s[14:15]
	s_andn2_b64 s[2:3], s[2:3], exec
	s_and_b64 s[0:1], s[0:1], exec
	s_or_b64 s[2:3], s[2:3], s[0:1]
	s_or_b64 exec, exec, s[16:17]
	s_and_saveexec_b64 s[14:15], s[2:3]
	v_mov_b32_e32 v5, v6
	v_mov_b32_e32 v3, v6
	v_mov_b32_e32 v2, v7
	s_or_b64 exec, exec, s[14:15]
	v_mov_b32_e32 v6, v1
	v_mov_b32_e32 v7, v1
	s_nop 0
	v_mov_b32_dpp v6, v5 row_ror:8 row_mask:0xf bank_mask:0xf
	v_mov_b32_dpp v7, v2 row_ror:8 row_mask:0xf bank_mask:0xf
	v_cmp_lt_f32_e64 s[2:3], v3, v6
	v_cmp_nlt_f32_e32 vcc, v3, v6
	s_and_saveexec_b64 s[16:17], vcc
	v_cmp_eq_f32_e32 vcc, v3, v6
	v_cmp_lt_i32_e64 s[14:15], v7, v2
	s_and_b64 s[0:1], vcc, s[14:15]
	s_andn2_b64 s[2:3], s[2:3], exec
	s_and_b64 s[0:1], s[0:1], exec
	s_or_b64 s[2:3], s[2:3], s[0:1]
	s_or_b64 exec, exec, s[16:17]
	s_and_saveexec_b64 s[14:15], s[2:3]
	v_mov_b32_e32 v5, v6
	v_mov_b32_e32 v3, v6
	v_mov_b32_e32 v2, v7
	s_or_b64 exec, exec, s[14:15]
	ds_bpermute_b32 v5, v148, v5
	ds_bpermute_b32 v6, v148, v2
	s_waitcnt lgkmcnt(1)
	v_cmp_lt_f32_e64 s[2:3], v3, v5
	v_cmp_nlt_f32_e32 vcc, v3, v5
	s_and_saveexec_b64 s[16:17], vcc
	s_cbranch_execz .LBB0_1058
	v_cmp_eq_f32_e32 vcc, v3, v5
	s_waitcnt lgkmcnt(0)
	v_cmp_lt_i32_e64 s[14:15], v6, v2
	s_and_b64 s[0:1], vcc, s[14:15]
	s_andn2_b64 s[2:3], s[2:3], exec
	s_and_b64 s[0:1], s[0:1], exec
	s_or_b64 s[2:3], s[2:3], s[0:1]
